# V^T image rows stored permuted by the V^T GEMM epilogue so each lane of the P.V tiles owns 4 consecutive value columns; attention epilogue writes 16 dwordx2 stores per lane instead of 64 short stores
# baseline (speedup 1.0000x reference)
; #define PG8_STAGE_B(bufoff, gbase) do { _Pragma("unroll") for (int _i = 0; _i < 2; ++_i) \
;         __builtin_amdgcn_global_load_lds((const unsigned*)((const char*)(gbase) + voffB[_i]), (LAS unsigned*)(lds + (bufoff) + ldsw + _i * 8192), 16, 0, 0); } while (0)
; #define PG8_STAGE_A(bufoff, gbase, UA) do { _Pragma("unroll") for (int _i = 0; _i < 2; ++_i) \
;         __builtin_amdgcn_global_load_lds((const unsigned*)((const char*)(gbase) + (UA)[_i]), (LAS unsigned*)(lds + (bufoff) + ldsw + _i * 8192), 16, 0, 0); } while (0)
; #define PG8_WAIT_V(n) asm volatile("s_waitcnt vmcnt(" #n ")" ::: "memory")
; #define PG8_BAR __builtin_amdgcn_s_barrier()
; template <class Epi, class Sched, bool GATHER, bool FP8 = false>
; __device__ __forceinline__ void gemm_phase(LAS unsigned char* lds, const Gemm g, const Sched& S, const Epi& E, const int wave_s) {
;     ...
;     const char* cB = (const char*)g.Bt + (size_t)cur.pn * tstepB;
;     PG8_STAGE_B(PG8_SB(0, 0), cB); PG8_STAGE_B(PG8_SB(0, 1), cB + hstepB); PG8_STAGE_A(PG8_SA(0, 0), cA, uAc[0]); PG8_STAGE_A(PG8_SA(0, 1), cA, uAc[1]);
;     if (wr == 1) PG8_BAR;
;     PG8_WAIT_V(2); PG8_BAR;
;     PG8_STAGE_B(PG8_SB(1, 0), cB + kstep); PG8_STAGE_A(PG8_SA(1, 0), cA + kstep, uAc[0]); PG8_STAGE_B(PG8_SB(1, 1), cB + hstepB + kstep);
;     PG8_WAIT_V(6); PG8_BAR;
;     __device__ __forceinline__ void operator()(const f32x4 (&acc)[2][2][4][2], const Unit& u, int wr, int wc, int fr, int fq) const {
;         const int row0 = u.pm * BM + wr * 64 + fr, col0 = u.pn * BM + wc * 32 + 8 * fq;
; #pragma unroll
;         for (int bj = 0; bj < 2; ++bj) {
;             const int n = col0 + bj * HALF;
;             const int b = (n < NCTX) ? (n >> 8) : ((n - NCTX) >> 13); const int key = (n < NCTX) ? (n & 255) : CTXL + ((n - NCTX) & 8191);
;             const int tile = key >> 6, kk0 = key & 63; const int boff = (kk0 >> 5) * 16 + 4 * ((kk0 & 31) >> 3);
; #pragma unroll
;             for (int ai = 0; ai < 2; ++ai)
; #pragma unroll
;                 for (int m = 0; m < 4; ++m) { const int vc = row0 + ai * HALF + m * 16; const int hh = vc >> 7, v = vc & 127;
;                     unsigned char* p = VT + ((size_t)((b * 4 + hh) * (KEYS / 64) + tile)) * VT_TILE + v * VT_ROW + boff;
.LBB0_463:
	v_lshrrev_b32_e32 v1, 1, v0
	v_and_b32_e32 v11, 24, v1
	v_readlane_b32 s46, v251, 24
	v_and_b32_e32 v10, 15, v0
	v_lshlrev_b32_e32 v1, 1, v11
	v_lshlrev_b32_e32 v0, 2, v0
	s_lshl_b32 s1, s1, 5
	v_mov_b32_e32 v131, v153
	v_readlane_b32 s47, v251, 25
	v_lshl_or_b32 v1, v10, 6, v1
	s_lshl_b32 s2, s10, 13
	v_and_b32_e32 v0, 32, v0
	s_and_b32 s1, s1, 0x60
	v_lshl_add_u64 v[2:3], s[46:47], 0, v[130:131]
	v_mov_b32_e32 v129, v153
	v_bitop3_b32 v12, v1, s2, v0 bitop3:0xde
	s_lshl_b32 s2, s1, 7
	v_lshl_add_u64 v[4:5], s[46:47], 0, v[128:129]
	v_mov_b32_e32 v133, v153
	v_bitop3_b32 v142, v1, s2, v0 bitop3:0xde
	s_add_i32 m0, s62, 0x18000
	v_lshl_add_u64 v[0:1], v[2:3], 0, s[96:97]
	v_lshl_add_u64 v[6:7], s[44:45], 0, v[132:133]
	v_mov_b32_e32 v135, v153
	s_waitcnt vmcnt(2)
	s_barrier
	global_load_lds_dwordx4 v[0:1], off
	v_lshl_add_u64 v[0:1], v[4:5], 0, s[96:97]
	s_add_i32 m0, s62, 0x1a000
	s_add_i32 s67, s62, 0x8000
	v_lshl_add_u64 v[8:9], s[44:45], 0, v[134:135]
	global_load_lds_dwordx4 v[0:1], off
	v_lshl_add_u64 v[0:1], v[6:7], 0, s[96:97]
	s_mov_b32 m0, s67
	s_add_i32 s68, s62, 0xa000
	v_readlane_b32 s2, v251, 26
	global_load_lds_dwordx4 v[0:1], off
	v_lshl_add_u64 v[0:1], v[8:9], 0, s[96:97]
	s_mov_b32 m0, s68
	v_readlane_b32 s3, v251, 27
	global_load_lds_dwordx4 v[0:1], off
	s_add_i32 m0, s62, 0x1c000
	v_lshl_add_u64 v[0:1], s[2:3], 0, v[130:131]
	global_load_lds_dwordx4 v[0:1], off
	v_lshl_add_u64 v[0:1], s[2:3], 0, v[128:129]
	s_add_i32 m0, s62, 0x1e000
	s_lshl_b32 s66, s10, 6
	global_load_lds_dwordx4 v[0:1], off
	s_waitcnt vmcnt(6)
	s_cmpk_lt_u32 s0, 0x100
	v_or_b32_e32 v143, s1, v11
	v_and_or_b32 v0, s66, 64, v10
	v_lshrrev_b32_e32 v140, 2, v0
	v_and_b32_e32 v141, 3, v0
	v_lshl_or_b32 v0, v141, 5, v140
	v_readlane_b32 s0, v251, 18
	v_mov_b32_e32 v137, v153
	v_mov_b32_e32 v139, v153
	s_cselect_b64 s[10:11], -1, 0
	v_mul_u32_u24_e32 v140, 0x50, v0
	v_mov_b32_e32 v141, v153
	s_mov_b32 s69, 0
	v_add_u32_e32 v144, 0, v12
	v_readlane_b32 s70, v251, 50
	s_mov_b32 s71, s0
	v_readlane_b32 s31, v251, 17
	s_barrier
	v_readlane_b32 s1, v251, 19
	s_branch .LBB0_466

; __device__ __forceinline__ unsigned pk4_fp8(float x0, float x1, float x2, float x3) { int w = 0; w = __builtin_amdgcn_cvt_pk_fp8_f32(x0, x1, w, false); w = __builtin_amdgcn_cvt_pk_fp8_f32(x2, x3, w, true); return (unsigned)w; }
;     __device__ __forceinline__ void operator()(const f32x4 (&acc)[2][2][4][2], const Unit& u, int wr, int wc, int fr, int fq) const {
;         const int row0 = u.pm * BM + wr * 64 + fr, col0 = u.pn * BM + wc * 32 + 8 * fq;
; #pragma unroll
;         for (int bj = 0; bj < 2; ++bj) {
;             const int n = col0 + bj * HALF;
;             const int b = (n < NCTX) ? (n >> 8) : ((n - NCTX) >> 13); const int key = (n < NCTX) ? (n & 255) : CTXL + ((n - NCTX) & 8191);
;             const int tile = key >> 6, kk0 = key & 63; const int boff = (kk0 >> 5) * 16 + 4 * ((kk0 & 31) >> 3);
; #pragma unroll
;             for (int ai = 0; ai < 2; ++ai)
; #pragma unroll
;                 for (int m = 0; m < 4; ++m) { const int vc = row0 + ai * HALF + m * 16; const int hh = vc >> 7, v = vc & 127;
;                     unsigned char* p = VT + ((size_t)((b * 4 + hh) * (KEYS / 64) + tile)) * VT_TILE + v * VT_ROW + boff;
;                     const f32x4 v0 = acc[ai][bj][m][0] * PV_Q, v1 = acc[ai][bj][m][1] * PV_Q;
;                     *(unsigned*)p = pk4_fp8(v0[0], v0[1], v0[2], v0[3]); *(unsigned*)(p + 32) = pk4_fp8(v1[0], v1[1], v1[2], v1[3]); } }
.LBB0_472:
	s_lshl_b32 s0, s71, 8
	s_add_i32 s1, s0, s66
	s_lshl_b32 s0, s70, 8
	v_or_b32_e32 v145, s0, v143
	v_add_u32_e32 v146, 0x1c00, v145
	s_movk_i32 s2, 0x400
	v_and_b32_e32 v146, 0x1f78, v146
	s_addk_i32 s0, 0xfc00
	v_cmp_gt_i32_e32 vcc, s2, v145
	v_add_u32_e32 v146, 0x100, v146
	s_lshr_b32 s0, s0, 13
	v_cndmask_b32_e32 v149, v146, v143, vcc
	v_mov_b32_e32 v147, s0
	v_mov_b32_e32 v154, s70
	v_lshrrev_b32_e32 v146, 6, v149
	v_lshrrev_b32_e32 v149, 1, v149
	v_cndmask_b32_e32 v148, v147, v154, vcc
	v_and_b32_e32 v152, 28, v149
	s_mov_b32 s4, 0x41000000
	v_lshlrev_b32_e32 v155, 2, v148
	v_lshl_add_u64 v[148:149], s[86:87], 0, v[152:153]
	v_pk_mul_f32 v[124:125], v[124:125], s[4:5] op_sel_hi:[1,0]
	v_cvt_pk_fp8_f32 v152, v124, v125
	v_pk_mul_f32 v[120:121], v[120:121], s[4:5] op_sel_hi:[1,0]
	v_mov_b32_e32 v124, v153
	v_cvt_pk_fp8_f32 v124, v120, v121
	v_pk_mul_f32 v[120:121], v[126:127], s[4:5] op_sel_hi:[1,0]
	v_pk_mul_f32 v[116:117], v[116:117], s[4:5] op_sel_hi:[1,0]
	v_cvt_pk_fp8_f32 v152, v120, v121 op_sel:[0,0,1]
	v_cvt_pk_fp8_f32 v120, v116, v117
	v_pk_mul_f32 v[112:113], v[112:113], s[4:5] op_sel_hi:[1,0]
	v_mov_b32_e32 v116, v153
	v_cvt_pk_fp8_f32 v116, v112, v113
	v_pk_mul_f32 v[112:113], v[118:119], s[4:5] op_sel_hi:[1,0]
	v_pk_mul_f32 v[108:109], v[108:109], s[4:5] op_sel_hi:[1,0]
	v_cvt_pk_fp8_f32 v120, v112, v113 op_sel:[0,0,1]
	v_cvt_pk_fp8_f32 v112, v108, v109
	v_pk_mul_f32 v[104:105], v[104:105], s[4:5] op_sel_hi:[1,0]
	v_mov_b32_e32 v108, v153
	v_cvt_pk_fp8_f32 v108, v104, v105
	v_pk_mul_f32 v[104:105], v[110:111], s[4:5] op_sel_hi:[1,0]
	v_pk_mul_f32 v[100:101], v[100:101], s[4:5] op_sel_hi:[1,0]
	v_cvt_pk_fp8_f32 v112, v104, v105 op_sel:[0,0,1]
	v_mov_b32_e32 v104, v153
	v_pk_mul_f32 v[96:97], v[96:97], s[4:5] op_sel_hi:[1,0]
	v_cvt_pk_fp8_f32 v104, v100, v101
	v_cvt_pk_fp8_f32 v100, v96, v97
	v_pk_mul_f32 v[98:99], v[98:99], s[4:5] op_sel_hi:[1,0]
	v_pk_mul_f32 v[92:93], v[92:93], s[4:5] op_sel_hi:[1,0]
	v_pk_mul_f32 v[88:89], v[88:89], s[4:5] op_sel_hi:[1,0]
	v_cvt_pk_fp8_f32 v100, v98, v99 op_sel:[0,0,1]
	v_cvt_pk_fp8_f32 v98, v92, v93
	v_mov_b32_e32 v92, v153
	v_cvt_pk_fp8_f32 v92, v88, v89
	v_pk_mul_f32 v[88:89], v[94:95], s[4:5] op_sel_hi:[1,0]
	v_pk_mul_f32 v[84:85], v[84:85], s[4:5] op_sel_hi:[1,0]
	v_cvt_pk_fp8_f32 v98, v88, v89 op_sel:[0,0,1]
	v_cvt_pk_fp8_f32 v88, v84, v85
	v_pk_mul_f32 v[80:81], v[80:81], s[4:5] op_sel_hi:[1,0]
	v_mov_b32_e32 v84, v153
	v_cvt_pk_fp8_f32 v84, v80, v81
	v_pk_mul_f32 v[80:81], v[86:87], s[4:5] op_sel_hi:[1,0]
	v_pk_mul_f32 v[76:77], v[76:77], s[4:5] op_sel_hi:[1,0]
	v_cvt_pk_fp8_f32 v88, v80, v81 op_sel:[0,0,1]
	v_cvt_pk_fp8_f32 v80, v76, v77
	v_pk_mul_f32 v[72:73], v[72:73], s[4:5] op_sel_hi:[1,0]
	v_cvt_pk_fp8_f32 v76, v72, v73
	v_pk_mul_f32 v[72:73], v[78:79], s[4:5] op_sel_hi:[1,0]
	v_pk_mul_f32 v[60:61], v[60:61], s[4:5] op_sel_hi:[1,0]
	v_cvt_pk_fp8_f32 v80, v72, v73 op_sel:[0,0,1]
	v_pk_mul_f32 v[56:57], v[56:57], s[4:5] op_sel_hi:[1,0]
	v_cvt_pk_fp8_f32 v72, v60, v61
	v_cvt_pk_fp8_f32 v60, v56, v57
	v_pk_mul_f32 v[56:57], v[62:63], s[4:5] op_sel_hi:[1,0]
	v_pk_mul_f32 v[62:63], v[68:69], s[4:5] op_sel_hi:[1,0]
	v_cvt_pk_fp8_f32 v68, v62, v63
	v_pk_mul_f32 v[62:63], v[70:71], s[4:5] op_sel_hi:[1,0]
	v_pk_mul_f32 v[52:53], v[52:53], s[4:5] op_sel_hi:[1,0]
	v_pk_mul_f32 v[48:49], v[48:49], s[4:5] op_sel_hi:[1,0]
	v_cvt_pk_fp8_f32 v68, v62, v63 op_sel:[0,0,1]
	v_cvt_pk_fp8_f32 v62, v52, v53
	v_mov_b32_e32 v52, v153
	v_cvt_pk_fp8_f32 v52, v48, v49
	v_pk_mul_f32 v[48:49], v[54:55], s[4:5] op_sel_hi:[1,0]
	v_pk_mul_f32 v[44:45], v[44:45], s[4:5] op_sel_hi:[1,0]
	v_cvt_pk_fp8_f32 v62, v48, v49 op_sel:[0,0,1]
	v_cvt_pk_fp8_f32 v48, v44, v45
	v_pk_mul_f32 v[40:41], v[40:41], s[4:5] op_sel_hi:[1,0]
	v_mov_b32_e32 v44, v153
	v_cvt_pk_fp8_f32 v44, v40, v41
	v_pk_mul_f32 v[40:41], v[46:47], s[4:5] op_sel_hi:[1,0]
	v_pk_mul_f32 v[36:37], v[36:37], s[4:5] op_sel_hi:[1,0]
	v_cvt_pk_fp8_f32 v48, v40, v41 op_sel:[0,0,1]
	v_mov_b32_e32 v40, v153
	v_pk_mul_f32 v[32:33], v[32:33], s[4:5] op_sel_hi:[1,0]
	v_cvt_pk_fp8_f32 v40, v36, v37
	v_cvt_pk_fp8_f32 v36, v32, v33
	v_pk_mul_f32 v[34:35], v[34:35], s[4:5] op_sel_hi:[1,0]
	v_pk_mul_f32 v[12:13], v[12:13], s[4:5] op_sel_hi:[1,0]
	s_ashr_i32 s0, s1, 7
	v_cvt_pk_fp8_f32 v36, v34, v35 op_sel:[0,0,1]
	v_cvt_pk_fp8_f32 v34, v12, v13
	s_addk_i32 s1, 0x80
	v_pk_mul_f32 v[58:59], v[58:59], s[4:5] op_sel_hi:[1,0]
	v_pk_mul_f32 v[96:97], v[102:103], s[4:5] op_sel_hi:[1,0]
	s_ashr_i32 s1, s1, 7
	v_cvt_pk_fp8_f32 v72, v56, v57 op_sel:[0,0,1]
	v_cvt_pk_fp8_f32 v60, v58, v59 op_sel:[0,0,1]
	v_or_b32_e32 v56, 0x80, v145
	v_add_u32_e32 v58, 0x1c80, v145
	v_pk_mul_f32 v[8:9], v[8:9], s[4:5] op_sel_hi:[1,0]
	v_add_u32_e32 v150, s0, v155
	v_pk_mul_f32 v[122:123], v[122:123], s[4:5] op_sel_hi:[1,0]
	v_pk_mul_f32 v[106:107], v[106:107], s[4:5] op_sel_hi:[1,0]
	v_cvt_pk_fp8_f32 v104, v96, v97 op_sel:[0,0,1]
	v_add_u32_e32 v96, s1, v155
	v_pk_mul_f32 v[90:91], v[90:91], s[4:5] op_sel_hi:[1,0]
	v_pk_mul_f32 v[74:75], v[74:75], s[4:5] op_sel_hi:[1,0]
	v_cmp_gt_i32_e32 vcc, s2, v56
	v_mov_b32_e32 v56, 0x80
	s_movk_i32 s2, 0xf8
	v_and_b32_e32 v58, 0x1ff8, v58
; __device__ __forceinline__ unsigned pk4_fp8(float x0, float x1, float x2, float x3) { int w = 0; w = __builtin_amdgcn_cvt_pk_fp8_f32(x0, x1, w, false); w = __builtin_amdgcn_cvt_pk_fp8_f32(x2, x3, w, true); return (unsigned)w; }
;     __device__ __forceinline__ void operator()(const f32x4 (&acc)[2][2][4][2], const Unit& u, int wr, int wc, int fr, int fq) const {
;     ...
;             for (int ai = 0; ai < 2; ++ai)
; #pragma unroll
;                 for (int m = 0; m < 4; ++m) { const int vc = row0 + ai * HALF + m * 16; const int hh = vc >> 7, v = vc & 127;
;                     unsigned char* p = VT + ((size_t)((b * 4 + hh) * (KEYS / 64) + tile)) * VT_TILE + v * VT_ROW + boff;
;                     const f32x4 v0 = acc[ai][bj][m][0] * PV_Q, v1 = acc[ai][bj][m][1] * PV_Q;
;                     *(unsigned*)p = pk4_fp8(v0[0], v0[1], v0[2], v0[3]); *(unsigned*)(p + 32) = pk4_fp8(v1[0], v1[1], v1[2], v1[3]); } }
	v_pk_mul_f32 v[64:65], v[64:65], s[4:5] op_sel_hi:[1,0]
	v_cvt_pk_fp8_f32 v12, v8, v9
	v_pk_mul_f32 v[8:9], v[14:15], s[4:5] op_sel_hi:[1,0]
	v_mad_u64_u32 v[150:151], s[40:41], v150, s83, v[146:147]
	s_movk_i32 s3, 0x2800
	v_cvt_pk_fp8_f32 v124, v122, v123 op_sel:[0,0,1]
	v_cvt_pk_fp8_f32 v108, v106, v107 op_sel:[0,0,1]
	v_mad_u64_u32 v[96:97], s[40:41], v96, s83, v[146:147]
	v_cvt_pk_fp8_f32 v92, v90, v91 op_sel:[0,0,1]
	v_cvt_pk_fp8_f32 v76, v74, v75 op_sel:[0,0,1]
	v_bitop3_b32 v56, v145, s2, v56 bitop3:0xc8
	v_add_u32_e32 v58, 0x100, v58
	v_cvt_pk_fp8_f32 v69, v64, v65
	v_cvt_pk_fp8_f32 v34, v8, v9 op_sel:[0,0,1]
	v_pk_mul_f32 v[4:5], v[4:5], s[4:5] op_sel_hi:[1,0]
	v_mad_i64_i32 v[150:151], s[40:41], v150, s3, v[148:149]
	v_pk_mul_f32 v[114:115], v[114:115], s[4:5] op_sel_hi:[1,0]
	v_mad_i64_i32 v[96:97], s[40:41], v96, s3, v[148:149]
	v_pk_mul_f32 v[82:83], v[82:83], s[4:5] op_sel_hi:[1,0]
	v_cndmask_b32_e32 v57, v147, v154, vcc
	v_cndmask_b32_e32 v58, v58, v56, vcc
	v_pk_mul_f32 v[0:1], v[0:1], s[4:5] op_sel_hi:[1,0]
	v_cvt_pk_fp8_f32 v8, v4, v5
	v_lshl_add_u64 v[150:151], v[150:151], 0, v[140:141]
	v_cvt_pk_fp8_f32 v116, v114, v115 op_sel:[0,0,1]
	v_lshl_add_u64 v[96:97], v[96:97], 0, v[140:141]
	v_cvt_pk_fp8_f32 v84, v82, v83 op_sel:[0,0,1]
	v_lshrrev_b32_e32 v56, 6, v58
	v_lshrrev_b32_e32 v58, 1, v58
	v_lshlrev_b32_e32 v57, 2, v57
	v_pk_mul_f32 v[32:33], v[38:39], s[4:5] op_sel_hi:[1,0]
	v_cvt_pk_fp8_f32 v4, v0, v1
	global_store_dword v[150:151], v152, off
	global_store_dword v[150:151], v124, off offset:32
	global_store_dword v[150:151], v120, off offset:320
	global_store_dword v[150:151], v116, off offset:352
	global_store_dword v[150:151], v112, off offset:640
	global_store_dword v[150:151], v108, off offset:672
	global_store_dword v[150:151], v104, off offset:960
	global_store_dword v[150:151], v100, off offset:992
	global_store_dword v[96:97], v98, off
	global_store_dword v[96:97], v92, off offset:32
	global_store_dword v[96:97], v88, off offset:320
	global_store_dword v[96:97], v84, off offset:352
	global_store_dword v[96:97], v80, off offset:640
	global_store_dword v[96:97], v76, off offset:672
	global_store_dword v[96:97], v72, off offset:960
	global_store_dword v[96:97], v60, off offset:992
	v_and_b32_e32 v152, 28, v58
	v_add_u32_e32 v60, s0, v57
	v_pk_mul_f32 v[64:65], v[66:67], s[4:5] op_sel_hi:[1,0]
	v_pk_mul_f32 v[42:43], v[42:43], s[4:5] op_sel_hi:[1,0]
	v_cvt_pk_fp8_f32 v40, v32, v33 op_sel:[0,0,1]
	v_add_u32_e32 v32, s1, v57
	v_pk_mul_f32 v[10:11], v[10:11], s[4:5] op_sel_hi:[1,0]
	v_lshl_add_u64 v[58:59], s[86:87], 0, v[152:153]
	v_mad_u64_u32 v[60:61], s[40:41], v60, s83, v[56:57]
	v_cvt_pk_fp8_f32 v69, v64, v65 op_sel:[0,0,1]
	v_cvt_pk_fp8_f32 v44, v42, v43 op_sel:[0,0,1]
	v_mad_u64_u32 v[32:33], s[0:1], v32, s83, v[56:57]
	v_cvt_pk_fp8_f32 v12, v10, v11 op_sel:[0,0,1]
	v_pk_mul_f32 v[0:1], v[6:7], s[4:5] op_sel_hi:[1,0]
	v_mad_i64_i32 v[60:61], s[40:41], v60, s3, v[58:59]
	v_pk_mul_f32 v[50:51], v[50:51], s[4:5] op_sel_hi:[1,0]
	v_mad_i64_i32 v[32:33], s[0:1], v32, s3, v[58:59]
	v_pk_mul_f32 v[2:3], v[2:3], s[4:5] op_sel_hi:[1,0]
	v_cvt_pk_fp8_f32 v8, v0, v1 op_sel:[0,0,1]
	v_lshl_add_u64 v[60:61], v[60:61], 0, v[140:141]
	v_cvt_pk_fp8_f32 v52, v50, v51 op_sel:[0,0,1]
	v_lshl_add_u64 v[32:33], v[32:33], 0, v[140:141]
	v_cvt_pk_fp8_f32 v4, v2, v3 op_sel:[0,0,1]
	global_store_dword v[60:61], v68, off
	global_store_dword v[60:61], v69, off offset:32
	global_store_dword v[60:61], v62, off offset:320
	global_store_dword v[60:61], v52, off offset:352
	global_store_dword v[60:61], v48, off offset:640
	global_store_dword v[60:61], v44, off offset:672
	global_store_dword v[60:61], v40, off offset:960
	global_store_dword v[60:61], v36, off offset:992
	global_store_dword v[32:33], v34, off
	global_store_dword v[32:33], v12, off offset:32
	global_store_dword v[32:33], v8, off offset:320
	global_store_dword v[32:33], v4, off offset:352
	v_pk_mul_f32 v[0:1], v[24:25], s[4:5] op_sel_hi:[1,0]
	v_pk_mul_f32 v[2:3], v[28:29], s[4:5] op_sel_hi:[1,0]
	v_cvt_pk_fp8_f32 v4, v0, v1
	v_cvt_pk_fp8_f32 v5, v2, v3
	v_pk_mul_f32 v[0:1], v[26:27], s[4:5] op_sel_hi:[1,0]
	v_pk_mul_f32 v[2:3], v[30:31], s[4:5] op_sel_hi:[1,0]
	v_cvt_pk_fp8_f32 v4, v0, v1 op_sel:[0,0,1]
	v_pk_mul_f32 v[0:1], v[16:17], s[4:5] op_sel_hi:[1,0]
	v_cvt_pk_fp8_f32 v5, v2, v3 op_sel:[0,0,1]
	v_pk_mul_f32 v[2:3], v[20:21], s[4:5] op_sel_hi:[1,0]
	v_cvt_pk_fp8_f32 v6, v0, v1
	v_cvt_pk_fp8_f32 v7, v2, v3
	v_pk_mul_f32 v[0:1], v[18:19], s[4:5] op_sel_hi:[1,0]
	v_pk_mul_f32 v[2:3], v[22:23], s[4:5] op_sel_hi:[1,0]
	v_cvt_pk_fp8_f32 v6, v0, v1 op_sel:[0,0,1]
	v_readlane_b32 s72, v254, 26
	v_cvt_pk_fp8_f32 v7, v2, v3 op_sel:[0,0,1]
	s_andn2_b64 vcc, exec, s[42:43]
	s_mov_b64 s[0:1], -1
	v_readlane_b32 s73, v254, 27
	v_readlane_b32 s74, v254, 28
	v_readlane_b32 s76, v254, 29
	global_store_dword v[32:33], v4, off offset:640
	global_store_dword v[32:33], v5, off offset:672
	global_store_dword v[32:33], v6, off offset:960
	global_store_dword v[32:33], v7, off offset:992
	v_readlane_b32 s77, v254, 30
	s_cbranch_vccnz .LBB0_465
	s_andn2_b64 vcc, exec, s[8:9]
	s_cbranch_vccnz .LBB0_464
	s_barrier
	s_branch .LBB0_464

; __device__ __forceinline__ unsigned pk4_fp8(float x0, float x1, float x2, float x3) { int w = 0; w = __builtin_amdgcn_cvt_pk_fp8_f32(x0, x1, w, false); w = __builtin_amdgcn_cvt_pk_fp8_f32(x2, x3, w, true); return (unsigned)w; }
; __device__ __forceinline__ int crow(int r, int hi) { return (r & 3) + 8 * (r >> 2) + 4 * hi; }
; __device__ __forceinline__ void finishSM(f32x16& p0, f32x16& p1, float alpha, float& l_reg, v8i& pa) {
; #pragma unroll
;     for (int r = 0; r < 16; ++r) p1[r] = __builtin_amdgcn_exp2f(p1[r]);
;     float sa = p0[0] + p0[1], sb = p0[2] + p0[3], sc = p0[4] + p0[5], sd = p0[6] + p0[7];
;     sa += p0[8]; sb += p0[9]; sc += p0[10]; sd += p0[11]; sa += p0[12]; sb += p0[13]; sc += p0[14]; sd += p0[15];
; #pragma unroll
;     for (int r = 0; r < 16; r += 4) { sa += p1[r]; sb += p1[r + 1]; sc += p1[r + 2]; sd += p1[r + 3]; }
;     float ps = (sa + sb) + (sc + sd);
;     { auto rr = __builtin_amdgcn_permlane32_swap(__float_as_uint(ps), __float_as_uint(ps), false, false);
;       ps = __uint_as_float(rr[0]) + __uint_as_float(rr[1]); }
;     l_reg = l_reg * alpha + ps;
; #pragma unroll
;     for (int c = 0; c < 4; ++c) { pa[c] = (int)pk4_fp8(p0[4 * c], p0[4 * c + 1], p0[4 * c + 2], p0[4 * c + 3]);
;         pa[4 + c] = (int)pk4_fp8(p1[4 * c], p1[4 * c + 1], p1[4 * c + 2], p1[4 * c + 3]); }
; __device__ __forceinline__ void attn_unit(const bf16_t* Qb, const unsigned char* Kh, const unsigned char* Vh, bf16_t* Ob, int seq, int cbase, int lbase, int t0, const f32x2* atab, char* lds, const int wave_s) {
;     ...
;     pv_d0(o, VBASE(bj), pa, r32, hi);
;     if (hi == 0) li_l[r32] = l_reg; asm volatile("s_waitcnt lgkmcnt(0)" ::: "memory");
;     float rli[16];
; #pragma unroll
;     for (int r = 0; r < 16; ++r) rli[r] = 8.f * __builtin_amdgcn_rcpf(li_l[crow(r, hi)]);
;     bf16_t* Ow = Ob + (long)(wid * QBLK) * LDO;
.LBB0_577:
	v_exp_f32_e32 v118, v96
	v_exp_f32_e32 v119, v97
	v_exp_f32_e32 v112, v98
	v_exp_f32_e32 v113, v99
	v_exp_f32_e32 v116, v100
	v_exp_f32_e32 v117, v101
	v_exp_f32_e32 v114, v102
	v_exp_f32_e32 v115, v103
	v_exp_f32_e32 v102, v104
	v_exp_f32_e32 v103, v105
	v_exp_f32_e32 v96, v106
	v_exp_f32_e32 v97, v107
	v_exp_f32_e32 v100, v108
	v_exp_f32_e32 v101, v109
	v_exp_f32_e32 v98, v110
	v_exp_f32_e32 v99, v111
	v_exp_f32_e32 v126, v80
	v_exp_f32_e32 v127, v81
	v_exp_f32_e32 v120, v82
	v_exp_f32_e32 v121, v83
	v_exp_f32_e32 v124, v84
	v_exp_f32_e32 v125, v85
	v_exp_f32_e32 v122, v86
	v_exp_f32_e32 v123, v87
	v_add_f32_e32 v64, v119, v118
	v_add_f32_e32 v65, v113, v112
	v_add_f32_e32 v66, v117, v116
	v_add_f32_e32 v67, v115, v114
	v_exp_f32_e32 v110, v88
	v_exp_f32_e32 v111, v89
	v_exp_f32_e32 v104, v90
	v_exp_f32_e32 v105, v91
	v_add_f32_e32 v64, v102, v64
	v_add_f32_e32 v65, v103, v65
	v_add_f32_e32 v66, v96, v66
	v_add_f32_e32 v67, v97, v67
	v_exp_f32_e32 v108, v92
	v_exp_f32_e32 v109, v93
	v_exp_f32_e32 v106, v94
	v_exp_f32_e32 v107, v95
	v_add_f32_e32 v64, v100, v64
	v_add_f32_e32 v65, v101, v65
	v_add_f32_e32 v66, v98, v66
	v_add_f32_e32 v67, v99, v67
	v_add_f32_e32 v64, v126, v64
	v_add_f32_e32 v65, v65, v127
	v_add_f32_e32 v66, v66, v120
	v_add_f32_e32 v67, v67, v121
	v_add_f32_e32 v64, v124, v64
	v_add_f32_e32 v65, v125, v65
	v_add_f32_e32 v66, v122, v66
	v_add_f32_e32 v67, v123, v67
	v_add_f32_e32 v64, v110, v64
	v_add_f32_e32 v65, v111, v65
	v_add_f32_e32 v66, v104, v66
	v_add_f32_e32 v67, v105, v67
	v_add_f32_e32 v64, v108, v64
	v_add_f32_e32 v65, v109, v65
	v_add_f32_e32 v66, v106, v66
	v_add_f32_e32 v67, v107, v67
	v_add_f32_e32 v64, v65, v64
	v_add_f32_e32 v65, v66, v67
	v_add_f32_e32 v131, v65, v64
	v_mov_b32_e32 v132, v131
	s_nop 1
	v_permlane32_swap_b32_e32 v131, v132
	ds_read_b128 v[88:91], v176 offset:13312
	ds_read_b128 v[92:95], v176 offset:13328
	ds_read_b128 v[80:83], v176 offset:15872
	ds_read_b128 v[84:87], v176 offset:15888
	ds_read_b128 v[72:75], v176 offset:18432
	ds_read_b128 v[76:79], v176 offset:18448
	ds_read_b128 v[64:67], v176 offset:20992
	ds_read_b128 v[68:71], v176 offset:21008
	s_and_saveexec_b64 s[0:1], s[44:45]
	v_add_f32_e32 v128, v128, v129
	v_fmac_f32_e32 v128, v175, v184
	v_add_f32_e32 v129, v131, v132
	v_fmac_f32_e32 v129, v128, v130
	ds_write_b32 v174, v129
	s_or_b64 exec, exec, s[0:1]
	v_cvt_pk_fp8_f32 v128, v118, v119
	v_cvt_pk_fp8_f32 v132, v126, v127
	v_cvt_pk_fp8_f32 v129, v116, v117
	v_cvt_pk_fp8_f32 v133, v124, v125
	v_cvt_pk_fp8_f32 v130, v102, v103
	v_cvt_pk_fp8_f32 v134, v110, v111
	v_cvt_pk_fp8_f32 v131, v100, v101
	v_cvt_pk_fp8_f32 v135, v108, v109
	v_cvt_pk_fp8_f32 v128, v112, v113 op_sel:[0,0,1]
	v_cvt_pk_fp8_f32 v132, v120, v121 op_sel:[0,0,1]
	v_cvt_pk_fp8_f32 v129, v114, v115 op_sel:[0,0,1]
	v_cvt_pk_fp8_f32 v133, v122, v123 op_sel:[0,0,1]
	v_cvt_pk_fp8_f32 v130, v96, v97 op_sel:[0,0,1]
	v_cvt_pk_fp8_f32 v134, v104, v105 op_sel:[0,0,1]
	v_cvt_pk_fp8_f32 v131, v98, v99 op_sel:[0,0,1]
	v_cvt_pk_fp8_f32 v135, v106, v107 op_sel:[0,0,1]
	s_waitcnt lgkmcnt(0)
	v_readlane_b32 s0, v255, 18
	v_readlane_b32 s2, v253, 34
	s_waitcnt lgkmcnt(6)
	v_mfma_scale_f32_32x32x64_f8f6f4 v[0:15], v[128:135], v[88:95], v[0:15], v201, v201 op_sel_hi:[0,0,0]
	v_add_u32_e32 v88, s31, v173
	s_lshl_b32 s0, s0, 7
	v_readlane_b32 s3, v253, 35
	s_ashr_i32 s1, s0, 31
	s_lshl_b64 s[6:7], s[2:3], 11
	v_readlane_b32 s2, v248, 53
	v_readlane_b32 s3, v248, 54
	s_add_u32 s2, s2, s6
	s_addc_u32 s3, s3, s7
	s_lshl_b64 s[0:1], s[0:1], 1
	s_add_u32 s0, s2, s0
	s_addc_u32 s1, s3, s1
	v_readlane_b32 s2, v248, 32
	v_readlane_b32 s3, v248, 33
	s_add_u32 s0, s0, s2
	s_waitcnt lgkmcnt(4)
	v_mfma_scale_f32_32x32x64_f8f6f4 v[48:63], v[128:135], v[80:87], v[48:63], v201, v201 op_sel_hi:[0,0,0]
	ds_read_b128 v[80:83], v88
	ds_read_b128 v[84:87], v88 offset:32
	s_addc_u32 s1, s1, s3
	v_lshlrev_b32_e32 v152, 3, v155
	s_waitcnt lgkmcnt(1)
	v_rcp_f32_e32 v80, v80
	v_rcp_f32_e32 v81, v81
	v_rcp_f32_e32 v82, v82
	v_rcp_f32_e32 v83, v83
	v_mul_f32_e32 v80, 0x41000000, v80
	v_mul_f32_e32 v81, 0x41000000, v81
	v_mul_f32_e32 v82, 0x41000000, v82
	v_mul_f32_e32 v83, 0x41000000, v83
	v_mfma_scale_f32_32x32x64_f8f6f4 v[32:47], v[128:135], v[72:79], v[32:47], v201, v201 op_sel_hi:[0,0,0]
	ds_read_b128 v[72:75], v88 offset:64
	ds_read_b128 v[76:79], v88 offset:96
	s_waitcnt lgkmcnt(2)
	v_rcp_f32_e32 v84, v84
	v_rcp_f32_e32 v85, v85
	v_rcp_f32_e32 v86, v86
	s_waitcnt lgkmcnt(1)
	v_rcp_f32_e32 v73, v73
	v_rcp_f32_e32 v74, v74
	v_rcp_f32_e32 v75, v75
	v_mul_f32_e32 v84, 0x41000000, v84
	v_mul_f32_e32 v85, 0x41000000, v85
	v_mul_f32_e32 v86, 0x41000000, v86
	v_rcp_f32_e32 v87, v87
	v_rcp_f32_e32 v72, v72
	v_mul_f32_e32 v87, 0x41000000, v87
	v_mfma_scale_f32_32x32x64_f8f6f4 v[16:31], v[128:135], v[64:71], v[16:31], v201, v201 op_sel_hi:[0,0,0]
	s_waitcnt lgkmcnt(0)
; __device__ __forceinline__ unsigned f2bf(float f) { return pk2(f, 0.f) & 0xffffu; }
; __device__ __forceinline__ int crow(int r, int hi) { return (r & 3) + 8 * (r >> 2) + 4 * hi; }
; __device__ __forceinline__ void attn_unit(const bf16_t* Qb, const unsigned char* Kh, const unsigned char* Vh, bf16_t* Ob, int seq, int cbase, int lbase, int t0, const f32x2* atab, char* lds, const int wave_s) {
;     ...
;     for (int r = 0; r < 16; ++r) rli[r] = 8.f * __builtin_amdgcn_rcpf(li_l[crow(r, hi)]);
;     bf16_t* Ow = Ob + (long)(wid * QBLK) * LDO;
; #pragma unroll
;     for (int r = 0; r < 16; ++r) { const int orow = crow(r, hi);
; #pragma unroll
;         for (int d0 = 0; d0 < 4; ++d0) Ow[(long)orow * LDO + d0 * 32 + r32] = (bf16_t)f2bf(o[d0][r] * rli[r]); }
	v_rcp_f32_e32 v64, v76
	v_rcp_f32_e32 v65, v77
	v_rcp_f32_e32 v66, v78
	v_rcp_f32_e32 v67, v79
	v_mul_f32_e32 v68, 0x41000000, v73
	v_mul_f32_e32 v69, 0x41000000, v74
	v_mul_f32_e32 v70, 0x41000000, v75
	v_mul_f32_e32 v71, 0x41000000, v64
	v_mul_f32_e32 v73, 0x41000000, v65
	v_mul_f32_e32 v74, 0x41000000, v66
	v_mul_f32_e32 v75, 0x41000000, v67
	v_lshlrev_b32_e32 v64, 13, v172
	v_lshl_add_u64 v[66:67], s[0:1], 0, v[152:153]
	v_mov_b32_e32 v65, v153
	v_lshl_add_u64 v[64:65], v[66:67], 0, v[64:65]
	s_nop 4
	v_mul_f32_e32 v194, v0, v80
	v_mul_f32_e32 v195, v48, v80
	v_mul_f32_e32 v211, v32, v80
	v_mul_f32_e32 v212, v16, v80
	v_cvt_pk_bf16_f32 v186, v194, v195
	v_cvt_pk_bf16_f32 v187, v211, v212
	global_store_dwordx2 v[64:65], v[186:187], off
	v_mul_f32_e32 v213, v1, v81
	v_mul_f32_e32 v214, v49, v81
	v_mul_f32_e32 v215, v33, v81
	v_mul_f32_e32 v216, v17, v81
	v_cvt_pk_bf16_f32 v188, v213, v214
	v_cvt_pk_bf16_f32 v189, v215, v216
	global_store_dwordx2 v[64:65], v[188:189], off offset:2048
	s_movk_i32 s0, 0x1000
	v_add_co_u32_e32 v0, vcc, s0, v64
	s_movk_i32 s0, 0x4000
	s_nop 0
	v_addc_co_u32_e32 v1, vcc, 0, v65, vcc
	v_mul_f32_e32 v194, v2, v82
	v_mul_f32_e32 v195, v50, v82
	v_mul_f32_e32 v211, v34, v82
	v_mul_f32_e32 v212, v18, v82
	v_cvt_pk_bf16_f32 v190, v194, v195
	v_cvt_pk_bf16_f32 v191, v211, v212
	global_store_dwordx2 v[0:1], v[190:191], off
	v_mul_f32_e32 v213, v3, v83
	v_mul_f32_e32 v214, v51, v83
	v_mul_f32_e32 v215, v35, v83
	v_mul_f32_e32 v216, v19, v83
	v_cvt_pk_bf16_f32 v192, v213, v214
	v_cvt_pk_bf16_f32 v193, v215, v216
	global_store_dwordx2 v[0:1], v[192:193], off offset:2048
	v_add_co_u32_e32 v0, vcc, s0, v64
	s_movk_i32 s0, 0x5000
	s_nop 0
	v_addc_co_u32_e32 v1, vcc, 0, v65, vcc
	v_add_co_u32_e32 v2, vcc, s0, v64
	v_mul_f32_e32 v72, 0x41000000, v72
	s_nop 0
	v_addc_co_u32_e32 v3, vcc, 0, v65, vcc
	v_mul_f32_e32 v194, v4, v84
	v_mul_f32_e32 v195, v52, v84
	v_mul_f32_e32 v211, v36, v84
	v_mul_f32_e32 v212, v20, v84
	v_cvt_pk_bf16_f32 v186, v194, v195
	v_cvt_pk_bf16_f32 v187, v211, v212
	global_store_dwordx2 v[0:1], v[186:187], off
	v_mul_f32_e32 v213, v5, v85
	v_mul_f32_e32 v214, v53, v85
	v_mul_f32_e32 v215, v37, v85
	v_mul_f32_e32 v216, v21, v85
	v_cvt_pk_bf16_f32 v188, v213, v214
	v_cvt_pk_bf16_f32 v189, v215, v216
	global_store_dwordx2 v[0:1], v[188:189], off offset:2048
	v_mul_f32_e32 v194, v6, v86
	v_mul_f32_e32 v195, v54, v86
	v_mul_f32_e32 v211, v38, v86
	v_mul_f32_e32 v212, v22, v86
	v_cvt_pk_bf16_f32 v190, v194, v195
	v_cvt_pk_bf16_f32 v191, v211, v212
	global_store_dwordx2 v[2:3], v[190:191], off
	v_mul_f32_e32 v213, v7, v87
	v_mul_f32_e32 v214, v55, v87
	v_mul_f32_e32 v215, v39, v87
	v_mul_f32_e32 v216, v23, v87
	v_cvt_pk_bf16_f32 v192, v213, v214
	v_cvt_pk_bf16_f32 v193, v215, v216
	global_store_dwordx2 v[2:3], v[192:193], off offset:2048
	s_mov_b32 s0, 0x8000
	v_add_co_u32_e32 v0, vcc, s0, v64
	s_mov_b32 s0, 0x9000
	s_nop 0
	v_addc_co_u32_e32 v1, vcc, 0, v65, vcc
	v_add_co_u32_e32 v2, vcc, s0, v64
	s_mov_b32 s0, 0xc000
	s_nop 0
	v_addc_co_u32_e32 v3, vcc, 0, v65, vcc
	v_mul_f32_e32 v194, v8, v72
	v_mul_f32_e32 v195, v56, v72
	v_mul_f32_e32 v211, v40, v72
	v_mul_f32_e32 v212, v24, v72
	v_cvt_pk_bf16_f32 v186, v194, v195
	v_cvt_pk_bf16_f32 v187, v211, v212
	global_store_dwordx2 v[0:1], v[186:187], off
	v_mul_f32_e32 v213, v9, v68
	v_mul_f32_e32 v214, v57, v68
	v_mul_f32_e32 v215, v41, v68
	v_mul_f32_e32 v216, v25, v68
	v_cvt_pk_bf16_f32 v188, v213, v214
	v_cvt_pk_bf16_f32 v189, v215, v216
	global_store_dwordx2 v[0:1], v[188:189], off offset:2048
	v_mul_f32_e32 v194, v10, v69
	v_mul_f32_e32 v195, v58, v69
	v_mul_f32_e32 v211, v42, v69
	v_mul_f32_e32 v212, v26, v69
	v_cvt_pk_bf16_f32 v190, v194, v195
	v_cvt_pk_bf16_f32 v191, v211, v212
	global_store_dwordx2 v[2:3], v[190:191], off
	v_mul_f32_e32 v213, v11, v70
	v_mul_f32_e32 v214, v59, v70
	v_mul_f32_e32 v215, v43, v70
	v_mul_f32_e32 v216, v27, v70
	v_cvt_pk_bf16_f32 v192, v213, v214
	v_cvt_pk_bf16_f32 v193, v215, v216
	global_store_dwordx2 v[2:3], v[192:193], off offset:2048
	v_add_co_u32_e32 v0, vcc, s0, v64
	s_mov_b32 s0, 0xd000
	s_nop 0
	v_addc_co_u32_e32 v1, vcc, 0, v65, vcc
	v_add_co_u32_e32 v2, vcc, s0, v64
	s_nop 1
	v_addc_co_u32_e32 v3, vcc, 0, v65, vcc
	v_mul_f32_e32 v194, v12, v71
	v_mul_f32_e32 v195, v60, v71
	v_mul_f32_e32 v211, v44, v71
	v_mul_f32_e32 v212, v28, v71
	v_cvt_pk_bf16_f32 v186, v194, v195
	v_cvt_pk_bf16_f32 v187, v211, v212
	global_store_dwordx2 v[0:1], v[186:187], off
	v_mul_f32_e32 v213, v13, v73
	v_mul_f32_e32 v214, v61, v73
	v_mul_f32_e32 v215, v45, v73
	v_mul_f32_e32 v216, v29, v73
	v_cvt_pk_bf16_f32 v188, v213, v214
	v_cvt_pk_bf16_f32 v189, v215, v216
	global_store_dwordx2 v[0:1], v[188:189], off offset:2048
	v_mul_f32_e32 v194, v14, v74
	v_mul_f32_e32 v195, v62, v74
	v_mul_f32_e32 v211, v46, v74
	v_mul_f32_e32 v212, v30, v74
	v_cvt_pk_bf16_f32 v190, v194, v195
	v_cvt_pk_bf16_f32 v191, v211, v212
	global_store_dwordx2 v[2:3], v[190:191], off
	s_andn2_b64 vcc, exec, s[52:53]
	v_mul_f32_e32 v213, v15, v75
	v_mul_f32_e32 v214, v63, v75
	v_mul_f32_e32 v215, v47, v75
	v_mul_f32_e32 v216, v31, v75
	v_cvt_pk_bf16_f32 v192, v213, v214
	v_cvt_pk_bf16_f32 v193, v215, v216
	global_store_dwordx2 v[2:3], v[192:193], off offset:2048
	s_waitcnt vmcnt(63) expcnt(7) lgkmcnt(15)
	s_barrier
	s_cbranch_vccnz .LBB0_583
	s_waitcnt vmcnt(0)
	s_barrier
	s_and_saveexec_b64 s[0:1], s[40:41]
	s_cbranch_execz .LBB0_582
	v_readlane_b32 s2, v255, 17
	s_lshl_b32 s2, s2, 6
	s_add_i32 s6, s2, s62
	s_ashr_i32 s7, s6, 31
	s_lshl_b64 s[6:7], s[6:7], 2
	v_readlane_b32 s2, v248, 34
	s_add_u32 s6, s2, s6
	v_readlane_b32 s2, v248, 35
	s_addc_u32 s7, s2, s7
	buffer_wbl2 sc1
	s_waitcnt vmcnt(0)
	s_waitcnt vmcnt(0)
	global_atomic_add v153, v197, s[6:7]
